# v54 + RG-LRU pass 1: chunk-top wait leaves the previous chunk's summary store in flight (vmcnt(1) instead of 0), as done for pass 2
# baseline (speedup 1.0000x reference)
; #define LAS __attribute__((address_space(3)))
; #define LDS_BARRIER() do { asm volatile("s_waitcnt lgkmcnt(0)" ::: "memory"); __builtin_amdgcn_s_barrier(); asm volatile("" ::: "memory"); } while (0)
; __device__ __forceinline__ unsigned pk2(float lo, float hi) { return pg8::cvt_pk_bf16(lo, hi); }
; template <bool FINAL> __device__ __forceinline__ void rglru_pass(Frame& F) {
;     ...
;     for (int c = cg; c < nch; c += ncg) {
;         const int row0 = c < 256 ? c * 64 : ML + (c - 256) * 64;
;         LDS_BARRIER();
; #pragma unroll
;         for (int it = 0; it < 2; ++it) { const int id = F.tid + 512 * it, t = id >> 4, c8 = (id & 15) * 8;
;             float a[8];
;             { const f32x4 b0 = *(const LAS f32x4*)(CWL + 512 + c8), b1 = *(const LAS f32x4*)(CWL + 512 + c8 + 4);
;               a[0] = b0.x; a[1] = b0.y; a[2] = b0.z; a[3] = b0.w; a[4] = b1.x; a[5] = b1.y; a[6] = b1.z; a[7] = b1.w; }
; #pragma unroll
;             for (int tap = 0; tap < 4; ++tap) { const v4u x = xq[it][tap];
;                 const f32x4 w0 = *(const LAS f32x4*)(CWL + tap * 128 + c8), w1 = *(const LAS f32x4*)(CWL + tap * 128 + c8 + 4);
;                 a[0] += w0.x * bflo(x[0]); a[1] += w0.y * bfhi(x[0]); a[2] += w0.z * bflo(x[1]); a[3] += w0.w * bfhi(x[1]);
;                 a[4] += w1.x * bflo(x[2]); a[5] += w1.y * bfhi(x[2]); a[6] += w1.z * bflo(x[3]); a[7] += w1.w * bfhi(x[3]); }
;             *(LAS f32x4*)(XCF + t * 128 + c8) = (f32x4){a[0], a[1], a[2], a[3]}; *(LAS f32x4*)(XCF + t * 128 + c8 + 4) = (f32x4){a[4], a[5], a[6], a[7]};
;             v4u w; w.x = pk2(a[0], a[1]); w.y = pk2(a[2], a[3]); w.z = pk2(a[4], a[5]); w.w = pk2(a[6], a[7]);
;             *(LAS v4u*)(XCB + t * 272 + c8 * 2) = w; }
;         LDS_BARRIER();
;         if (c + ncg < nch) RG_LOAD_ROWS(c + ncg);
.LBB0_1392:
	s_waitcnt lgkmcnt(0)
	s_barrier
	s_waitcnt lgkmcnt(0)
	ds_read_b128 v[34:37], v167
	ds_read_b128 v[38:41], v167 offset:16
	ds_read_b128 v[42:45], v176
	ds_read_b128 v[46:49], v176 offset:16
	ds_read_b128 v[50:53], v176 offset:512
	ds_read_b128 v[54:57], v176 offset:528
	ds_read_b128 v[58:61], v176 offset:1024
	ds_read_b128 v[62:65], v176 offset:1040
	ds_read_b128 v[170:173], v176 offset:1536
	ds_read_b128 v[188:191], v176 offset:1552
	s_waitcnt vmcnt(1)
	v_lshlrev_b32_e32 v174, 16, v134
	v_and_b32_e32 v175, 0xffff0000, v134
	s_waitcnt lgkmcnt(7)
	v_pk_fma_f32 v[34:35], v[42:43], v[174:175], v[34:35]
	v_lshlrev_b32_e32 v42, 16, v130
	v_and_b32_e32 v43, 0xffff0000, v130
	s_waitcnt lgkmcnt(5)
	v_pk_fma_f32 v[34:35], v[50:51], v[42:43], v[34:35]
	v_lshlrev_b32_e32 v42, 16, v138
	v_and_b32_e32 v43, 0xffff0000, v138
	s_waitcnt lgkmcnt(3)
	v_pk_fma_f32 v[34:35], v[58:59], v[42:43], v[34:35]
	v_lshlrev_b32_e32 v42, 16, v142
	v_and_b32_e32 v43, 0xffff0000, v142
	s_waitcnt lgkmcnt(1)
	v_pk_fma_f32 v[34:35], v[170:171], v[42:43], v[34:35]
	v_lshlrev_b32_e32 v42, 16, v135
	v_and_b32_e32 v43, 0xffff0000, v135
	v_pk_fma_f32 v[36:37], v[44:45], v[42:43], v[36:37]
	v_lshlrev_b32_e32 v42, 16, v131
	v_and_b32_e32 v43, 0xffff0000, v131
	v_pk_fma_f32 v[36:37], v[52:53], v[42:43], v[36:37]
	v_lshlrev_b32_e32 v42, 16, v139
	v_and_b32_e32 v43, 0xffff0000, v139
	v_pk_fma_f32 v[36:37], v[60:61], v[42:43], v[36:37]
	v_lshlrev_b32_e32 v42, 16, v143
	v_and_b32_e32 v43, 0xffff0000, v143
	v_pk_fma_f32 v[36:37], v[172:173], v[42:43], v[36:37]
	v_lshlrev_b32_e32 v42, 16, v136
	v_and_b32_e32 v43, 0xffff0000, v136
	v_pk_fma_f32 v[38:39], v[46:47], v[42:43], v[38:39]
	v_lshlrev_b32_e32 v42, 16, v132
	v_and_b32_e32 v43, 0xffff0000, v132
	v_pk_fma_f32 v[38:39], v[54:55], v[42:43], v[38:39]
	v_lshlrev_b32_e32 v42, 16, v140
	v_and_b32_e32 v43, 0xffff0000, v140
	v_pk_fma_f32 v[38:39], v[62:63], v[42:43], v[38:39]
	v_lshlrev_b32_e32 v42, 16, v144
	v_and_b32_e32 v43, 0xffff0000, v144
	s_waitcnt lgkmcnt(0)
	v_pk_fma_f32 v[38:39], v[188:189], v[42:43], v[38:39]
	v_lshlrev_b32_e32 v42, 16, v137
	v_and_b32_e32 v43, 0xffff0000, v137
	v_pk_fma_f32 v[40:41], v[48:49], v[42:43], v[40:41]
	v_lshlrev_b32_e32 v42, 16, v133
	v_and_b32_e32 v43, 0xffff0000, v133
	v_pk_fma_f32 v[40:41], v[56:57], v[42:43], v[40:41]
	v_lshlrev_b32_e32 v42, 16, v141
	v_and_b32_e32 v43, 0xffff0000, v141
	v_pk_fma_f32 v[40:41], v[64:65], v[42:43], v[40:41]
	v_lshlrev_b32_e32 v42, 16, v145
	v_and_b32_e32 v43, 0xffff0000, v145
	v_pk_fma_f32 v[40:41], v[190:191], v[42:43], v[40:41]
	ds_write_b128 v177, v[34:37] offset:17408
	ds_write_b128 v177, v[38:41] offset:17424
	v_cvt_pk_bf16_f32 v34, v34, v35
	v_cvt_pk_bf16_f32 v35, v36, v37
	v_cvt_pk_bf16_f32 v36, v38, v39
	v_cvt_pk_bf16_f32 v37, v40, v41
	ds_write_b128 v182, v[34:37]
	ds_read_b128 v[34:37], v167
	ds_read_b128 v[38:41], v167 offset:16
	ds_read_b128 v[42:45], v176
	ds_read_b128 v[46:49], v176 offset:16
	ds_read_b128 v[50:53], v176 offset:512
	ds_read_b128 v[54:57], v176 offset:528
	ds_read_b128 v[58:61], v176 offset:1024
	ds_read_b128 v[62:65], v176 offset:1040
	ds_read_b128 v[170:173], v176 offset:1536
	ds_read_b128 v[188:191], v176 offset:1552
	v_lshlrev_b32_e32 v174, 16, v146
	v_and_b32_e32 v175, 0xffff0000, v146
	s_waitcnt lgkmcnt(7)
	v_pk_fma_f32 v[34:35], v[42:43], v[174:175], v[34:35]
	v_lshlrev_b32_e32 v42, 16, v150
	v_and_b32_e32 v43, 0xffff0000, v150
	s_waitcnt lgkmcnt(5)
	v_pk_fma_f32 v[34:35], v[50:51], v[42:43], v[34:35]
	v_lshlrev_b32_e32 v42, 16, v156
	v_and_b32_e32 v43, 0xffff0000, v156
	s_waitcnt lgkmcnt(3)
	v_pk_fma_f32 v[34:35], v[58:59], v[42:43], v[34:35]
	v_lshlrev_b32_e32 v42, 16, v160
	v_and_b32_e32 v43, 0xffff0000, v160
	s_waitcnt lgkmcnt(1)
	v_pk_fma_f32 v[34:35], v[170:171], v[42:43], v[34:35]
	v_lshlrev_b32_e32 v42, 16, v147
	v_and_b32_e32 v43, 0xffff0000, v147
	v_pk_fma_f32 v[36:37], v[44:45], v[42:43], v[36:37]
	v_lshlrev_b32_e32 v42, 16, v151
	v_and_b32_e32 v43, 0xffff0000, v151
	v_pk_fma_f32 v[36:37], v[52:53], v[42:43], v[36:37]
	v_lshlrev_b32_e32 v42, 16, v157
	v_and_b32_e32 v43, 0xffff0000, v157
	v_pk_fma_f32 v[36:37], v[60:61], v[42:43], v[36:37]
	v_lshlrev_b32_e32 v42, 16, v161
	v_and_b32_e32 v43, 0xffff0000, v161
	v_pk_fma_f32 v[36:37], v[172:173], v[42:43], v[36:37]
	v_lshlrev_b32_e32 v42, 16, v148
	v_and_b32_e32 v43, 0xffff0000, v148
	v_pk_fma_f32 v[38:39], v[46:47], v[42:43], v[38:39]
	v_lshlrev_b32_e32 v42, 16, v152
	v_and_b32_e32 v43, 0xffff0000, v152
	v_pk_fma_f32 v[38:39], v[54:55], v[42:43], v[38:39]
	v_lshlrev_b32_e32 v42, 16, v158
	v_and_b32_e32 v43, 0xffff0000, v158
	v_pk_fma_f32 v[38:39], v[62:63], v[42:43], v[38:39]
	v_lshlrev_b32_e32 v42, 16, v162
	v_and_b32_e32 v43, 0xffff0000, v162
	s_waitcnt lgkmcnt(0)
	v_pk_fma_f32 v[38:39], v[188:189], v[42:43], v[38:39]
	v_lshlrev_b32_e32 v42, 16, v149
	v_and_b32_e32 v43, 0xffff0000, v149
	v_pk_fma_f32 v[40:41], v[48:49], v[42:43], v[40:41]
	v_lshlrev_b32_e32 v42, 16, v153
	v_and_b32_e32 v43, 0xffff0000, v153
	v_pk_fma_f32 v[40:41], v[56:57], v[42:43], v[40:41]
	v_lshlrev_b32_e32 v42, 16, v159
	v_and_b32_e32 v43, 0xffff0000, v159
	v_pk_fma_f32 v[40:41], v[64:65], v[42:43], v[40:41]
	v_lshlrev_b32_e32 v42, 16, v163
	v_and_b32_e32 v43, 0xffff0000, v163
	v_pk_fma_f32 v[40:41], v[190:191], v[42:43], v[40:41]
	ds_write_b128 v181, v[34:37] offset:17408
	ds_write_b128 v181, v[38:41] offset:17424
	v_cvt_pk_bf16_f32 v34, v34, v35
	v_cvt_pk_bf16_f32 v35, v36, v37
	v_cvt_pk_bf16_f32 v36, v38, v39
	v_cvt_pk_bf16_f32 v37, v40, v41
	ds_write_b128 v183, v[34:37]
	s_add_i32 s12, s12, s14
	s_waitcnt lgkmcnt(0)
	s_barrier
	s_cmpk_gt_i32 s12, 0x107
	s_cselect_b64 s[22:23], -1, 0
	s_and_b64 vcc, exec, s[22:23]
	s_cbranch_vccnz .LBB0_1410
	s_cmpk_lt_i32 s12, 0x100
	s_cselect_b32 s7, s24, 0xffffff00
	s_cselect_b32 s6, s21, 0x100
	s_and_b32 s25, s7, s13
	s_mov_b32 s76, s25
	s_mov_b32 s77, 0
	s_lshl_b64 s[76:77], s[76:77], 13
	s_add_u32 s76, s76, 0x1000
	s_addc_u32 s77, s77, 0
	s_add_u32 s68, s8, s76
	s_addc_u32 s69, s9, s77
	s_and_b32 s69, s69, 0xffff
	s_lshl_b32 s70, s6, 13
	s_sub_u32 s70, s70, 0x1000
	s_mov_b32 s71, 0x20000
	s_sub_i32 s78, s13, s25
	s_add_i32 s78, s78, -2
	v_lshlrev_b32_e32 v38, 1, v166
	v_add_u32_e32 v34, s78, v1
	v_lshl_add_u32 v34, v34, 13, v38
	buffer_load_dwordx4 v[134:137], v34, s[68:71], 0 offen
	v_add_u32_e32 v35, 0x2000, v34
	buffer_load_dwordx4 v[130:133], v35, s[68:71], 0 offen
	v_add_u32_e32 v36, 0x4000, v34
	buffer_load_dwordx4 v[138:141], v36, s[68:71], 0 offen
	v_add_u32_e32 v37, 0x6000, v34
	buffer_load_dwordx4 v[142:145], v37, s[68:71], 0 offen
	v_add_u32_e32 v34, s78, v179
	v_lshl_add_u32 v34, v34, 13, v38
	buffer_load_dwordx4 v[146:149], v34, s[68:71], 0 offen
	v_add_u32_e32 v35, 0x2000, v34
	buffer_load_dwordx4 v[150:153], v35, s[68:71], 0 offen
	v_add_u32_e32 v36, 0x4000, v34
	buffer_load_dwordx4 v[156:159], v36, s[68:71], 0 offen
	v_add_u32_e32 v37, 0x6000, v34
	buffer_load_dwordx4 v[160:163], v37, s[68:71], 0 offen
	v_mov_b32_e32 v155, v154
